# conformer conv tap reads kept 12 deep instead of 8 (deeper software pipelining of the LDS reads)
# speedup vs baseline: 1.0077x; 1.0077x over previous
.LBB0_2165:
	ds_read_u16 v29, v22
	ds_read_u16 v30, v22 offset:1024
	ds_read_u16 v31, v22 offset:2048
	ds_read_u16 v32, v22 offset:3072
	ds_read_u16 v33, v22 offset:4096
	ds_read_u16 v34, v22 offset:5120
	ds_read_u16 v35, v22 offset:6144
	ds_read_u16 v36, v22 offset:7168
	s_waitcnt lgkmcnt(7)
	v_lshlrev_b32_e32 v29, 16, v29
	v_fma_f32 v29, v51, v29, v52
	s_waitcnt lgkmcnt(6)
	v_lshlrev_b32_e32 v30, 16, v30
	v_fmac_f32_e32 v29, v54, v30
	v_fma_f32 v30, v51, v30, v52
	s_waitcnt lgkmcnt(5)
	v_lshlrev_b32_e32 v31, 16, v31
	v_fmac_f32_e32 v29, v55, v31
	v_fmac_f32_e32 v30, v54, v31
	v_fma_f32 v31, v51, v31, v52
	s_waitcnt lgkmcnt(4)
	v_lshlrev_b32_e32 v32, 16, v32
	ds_read_u16 v37, v22 offset:8192
	ds_read_u16 v38, v22 offset:9216
	ds_read_u16 v39, v22 offset:10240
	ds_read_u16 v40, v22 offset:11264
	ds_read_u16 v41, v22 offset:12288
	ds_read_u16 v42, v22 offset:13312
	ds_read_u16 v43, v22 offset:14336
	ds_read_u16 v44, v22 offset:15360
	v_fmac_f32_e32 v29, v56, v32
	v_fmac_f32_e32 v30, v55, v32
	v_fmac_f32_e32 v31, v54, v32
	v_fma_f32 v32, v51, v32, v52
	s_waitcnt lgkmcnt(11)
	v_lshlrev_b32_e32 v33, 16, v33
	v_fmac_f32_e32 v29, v57, v33
	v_fmac_f32_e32 v30, v56, v33
	v_fmac_f32_e32 v31, v55, v33
	v_fmac_f32_e32 v32, v54, v33
	v_fma_f32 v33, v51, v33, v52
	s_waitcnt lgkmcnt(10)
	v_lshlrev_b32_e32 v34, 16, v34
	v_fmac_f32_e32 v29, v58, v34
	v_fmac_f32_e32 v30, v57, v34
	v_fmac_f32_e32 v31, v56, v34
	v_fmac_f32_e32 v32, v55, v34
	v_fmac_f32_e32 v33, v54, v34
	v_fma_f32 v34, v51, v34, v52
	s_waitcnt lgkmcnt(9)
	v_lshlrev_b32_e32 v35, 16, v35
	v_fmac_f32_e32 v29, v59, v35
	v_fmac_f32_e32 v30, v58, v35
	v_fmac_f32_e32 v31, v57, v35
	v_fmac_f32_e32 v32, v56, v35
	v_fmac_f32_e32 v33, v55, v35
	v_fmac_f32_e32 v34, v54, v35
	v_fma_f32 v35, v51, v35, v52
	s_waitcnt lgkmcnt(8)
	v_lshlrev_b32_e32 v36, 16, v36
	v_fmac_f32_e32 v29, v60, v36
	v_fmac_f32_e32 v30, v59, v36
	v_fmac_f32_e32 v31, v58, v36
	v_fmac_f32_e32 v32, v57, v36
	v_fmac_f32_e32 v33, v56, v36
	v_fmac_f32_e32 v34, v55, v36
	v_fmac_f32_e32 v35, v54, v36
	v_fma_f32 v36, v51, v36, v52
	s_waitcnt lgkmcnt(7)
	v_lshlrev_b32_e32 v37, 16, v37
	v_fmac_f32_e32 v29, v61, v37
	v_fmac_f32_e32 v30, v60, v37
	v_fmac_f32_e32 v31, v59, v37
	v_fmac_f32_e32 v32, v58, v37
	v_fmac_f32_e32 v33, v57, v37
	v_fmac_f32_e32 v34, v56, v37
	v_fmac_f32_e32 v35, v55, v37
	v_fmac_f32_e32 v36, v54, v37
	v_fma_f32 v37, v51, v37, v52
	s_waitcnt lgkmcnt(6)
	v_lshlrev_b32_e32 v38, 16, v38
	v_fmac_f32_e32 v29, v62, v38
	v_fmac_f32_e32 v30, v61, v38
	v_fmac_f32_e32 v31, v60, v38
	v_fmac_f32_e32 v32, v59, v38
	v_fmac_f32_e32 v33, v58, v38
	v_fmac_f32_e32 v34, v57, v38
	v_fmac_f32_e32 v35, v56, v38
	v_fmac_f32_e32 v36, v55, v38
	v_fmac_f32_e32 v37, v54, v38
	v_fma_f32 v38, v51, v38, v52
	s_waitcnt lgkmcnt(5)
	v_lshlrev_b32_e32 v39, 16, v39
	v_fmac_f32_e32 v29, v63, v39
	v_fmac_f32_e32 v30, v62, v39
	v_fmac_f32_e32 v31, v61, v39
	v_fmac_f32_e32 v32, v60, v39
	v_fmac_f32_e32 v33, v59, v39
	v_fmac_f32_e32 v34, v58, v39
	v_fmac_f32_e32 v35, v57, v39
	v_fmac_f32_e32 v36, v56, v39
	v_fmac_f32_e32 v37, v55, v39
	v_fmac_f32_e32 v38, v54, v39
	v_fma_f32 v39, v51, v39, v52
	s_waitcnt lgkmcnt(4)
	v_lshlrev_b32_e32 v40, 16, v40
	ds_read_u16 v45, v22 offset:16384
	v_fmac_f32_e32 v29, v64, v40
	v_fmac_f32_e32 v30, v63, v40
	v_fmac_f32_e32 v31, v62, v40
	v_fmac_f32_e32 v32, v61, v40
	v_fmac_f32_e32 v33, v60, v40
	v_fmac_f32_e32 v34, v59, v40
	v_fmac_f32_e32 v35, v58, v40
	v_fmac_f32_e32 v36, v57, v40
	v_fmac_f32_e32 v37, v56, v40
	v_fmac_f32_e32 v38, v55, v40
	v_fmac_f32_e32 v39, v54, v40
	v_fma_f32 v40, v51, v40, v52
	s_waitcnt lgkmcnt(4)
	v_lshlrev_b32_e32 v41, 16, v41
	v_fmac_f32_e32 v29, v65, v41
	v_fmac_f32_e32 v30, v64, v41
	v_fmac_f32_e32 v31, v63, v41
	v_fmac_f32_e32 v32, v62, v41
	v_fmac_f32_e32 v33, v61, v41
	v_fmac_f32_e32 v34, v60, v41
	v_fmac_f32_e32 v35, v59, v41
	v_fmac_f32_e32 v36, v58, v41
	v_fmac_f32_e32 v37, v57, v41
	v_fmac_f32_e32 v38, v56, v41
	v_fmac_f32_e32 v39, v55, v41
	v_fmac_f32_e32 v40, v54, v41
	v_fma_f32 v41, v51, v41, v52
	s_waitcnt lgkmcnt(3)
	v_lshlrev_b32_e32 v42, 16, v42
	v_fmac_f32_e32 v29, v66, v42
	v_fmac_f32_e32 v30, v65, v42
	v_fmac_f32_e32 v31, v64, v42
	v_fmac_f32_e32 v32, v63, v42
	v_fmac_f32_e32 v33, v62, v42
	v_fmac_f32_e32 v34, v61, v42
	v_fmac_f32_e32 v35, v60, v42
	v_fmac_f32_e32 v36, v59, v42
	v_fmac_f32_e32 v37, v58, v42
	v_fmac_f32_e32 v38, v57, v42
	v_fmac_f32_e32 v39, v56, v42
	v_fmac_f32_e32 v40, v55, v42
	v_fmac_f32_e32 v41, v54, v42
	v_fma_f32 v42, v51, v42, v52
	s_waitcnt lgkmcnt(2)
	v_lshlrev_b32_e32 v43, 16, v43
	v_fmac_f32_e32 v29, v67, v43
	v_fmac_f32_e32 v30, v66, v43
	v_fmac_f32_e32 v31, v65, v43
	v_fmac_f32_e32 v32, v64, v43
	v_fmac_f32_e32 v33, v63, v43
	v_fmac_f32_e32 v34, v62, v43
	v_fmac_f32_e32 v35, v61, v43
	v_fmac_f32_e32 v36, v60, v43
	v_fmac_f32_e32 v37, v59, v43
	v_fmac_f32_e32 v38, v58, v43
	v_fmac_f32_e32 v39, v57, v43
	v_fmac_f32_e32 v40, v56, v43
	v_fmac_f32_e32 v41, v55, v43
	v_fmac_f32_e32 v42, v54, v43
	v_fma_f32 v43, v51, v43, v52
	s_waitcnt lgkmcnt(1)
	v_lshlrev_b32_e32 v44, 16, v44
	v_fmac_f32_e32 v29, v68, v44
	v_fmac_f32_e32 v30, v67, v44
	v_fmac_f32_e32 v31, v66, v44
	v_fmac_f32_e32 v32, v65, v44
	v_fmac_f32_e32 v33, v64, v44
	v_fmac_f32_e32 v34, v63, v44
	v_fmac_f32_e32 v35, v62, v44
	v_fmac_f32_e32 v36, v61, v44
	v_fmac_f32_e32 v37, v60, v44
	v_fmac_f32_e32 v38, v59, v44
	v_fmac_f32_e32 v39, v58, v44
	v_fmac_f32_e32 v40, v57, v44
	v_fmac_f32_e32 v41, v56, v44
	v_fmac_f32_e32 v42, v55, v44
	v_fmac_f32_e32 v43, v54, v44
	v_fma_f32 v44, v51, v44, v52
	s_waitcnt lgkmcnt(0)
	v_lshlrev_b32_e32 v45, 16, v45
	v_fmac_f32_e32 v29, v69, v45
	v_fmac_f32_e32 v30, v68, v45
	v_fmac_f32_e32 v31, v67, v45
	v_fmac_f32_e32 v32, v66, v45
	v_fmac_f32_e32 v33, v65, v45
	v_fmac_f32_e32 v34, v64, v45
	v_fmac_f32_e32 v35, v63, v45
	v_fmac_f32_e32 v36, v62, v45
	v_fmac_f32_e32 v37, v61, v45
	v_fmac_f32_e32 v38, v60, v45
	v_fmac_f32_e32 v39, v59, v45
	v_fmac_f32_e32 v40, v58, v45
	v_fmac_f32_e32 v41, v57, v45
	v_fmac_f32_e32 v42, v56, v45
	v_fmac_f32_e32 v43, v55, v45
	v_fmac_f32_e32 v44, v54, v45
	ds_read_u16 v100, v22 offset:17408
	ds_read_u16 v101, v22 offset:18432
	ds_read_u16 v102, v22 offset:19456
	ds_read_u16 v103, v22 offset:20480
	ds_read_u16 v104, v22 offset:21504
	ds_read_u16 v105, v22 offset:22528
	ds_read_u16 v106, v22 offset:23552
	ds_read_u16 v107, v22 offset:24576
	ds_read_u16 v108, v22 offset:25600
	ds_read_u16 v109, v22 offset:26624
	ds_read_u16 v110, v22 offset:27648
	ds_read_u16 v111, v22 offset:28672
	s_waitcnt lgkmcnt(11)
	v_lshlrev_b32_e32 v45, 16, v100
	ds_read_u16 v100, v22 offset:29696
	v_fmac_f32_e32 v29, v70, v45
	v_fmac_f32_e32 v30, v69, v45
	v_fmac_f32_e32 v31, v68, v45
	v_fmac_f32_e32 v32, v67, v45
	v_fmac_f32_e32 v33, v66, v45
	v_fmac_f32_e32 v34, v65, v45
	v_fmac_f32_e32 v35, v64, v45
	v_fmac_f32_e32 v36, v63, v45
	v_fmac_f32_e32 v37, v62, v45
	v_fmac_f32_e32 v38, v61, v45
	v_fmac_f32_e32 v39, v60, v45
	v_fmac_f32_e32 v40, v59, v45
	v_fmac_f32_e32 v41, v58, v45
	v_fmac_f32_e32 v42, v57, v45
	v_fmac_f32_e32 v43, v56, v45
	v_fmac_f32_e32 v44, v55, v45
	s_waitcnt lgkmcnt(11)
	v_lshlrev_b32_e32 v45, 16, v101
	ds_read_u16 v101, v22 offset:30720
	v_fmac_f32_e32 v29, v71, v45
	v_fmac_f32_e32 v30, v70, v45
	v_fmac_f32_e32 v31, v69, v45
	v_fmac_f32_e32 v32, v68, v45
	v_fmac_f32_e32 v33, v67, v45
	v_fmac_f32_e32 v34, v66, v45
	v_fmac_f32_e32 v35, v65, v45
	v_fmac_f32_e32 v36, v64, v45
	v_fmac_f32_e32 v37, v63, v45
	v_fmac_f32_e32 v38, v62, v45
	v_fmac_f32_e32 v39, v61, v45
	v_fmac_f32_e32 v40, v60, v45
	v_fmac_f32_e32 v41, v59, v45
	v_fmac_f32_e32 v42, v58, v45
	v_fmac_f32_e32 v43, v57, v45
	v_fmac_f32_e32 v44, v56, v45
	s_waitcnt lgkmcnt(11)
	v_lshlrev_b32_e32 v45, 16, v102
	ds_read_u16 v102, v22 offset:31744
	v_fmac_f32_e32 v29, v72, v45
	v_fmac_f32_e32 v30, v71, v45
	v_fmac_f32_e32 v31, v70, v45
	v_fmac_f32_e32 v32, v69, v45
	v_fmac_f32_e32 v33, v68, v45
	v_fmac_f32_e32 v34, v67, v45
	v_fmac_f32_e32 v35, v66, v45
	v_fmac_f32_e32 v36, v65, v45
	v_fmac_f32_e32 v37, v64, v45
	v_fmac_f32_e32 v38, v63, v45
	v_fmac_f32_e32 v39, v62, v45
	v_fmac_f32_e32 v40, v61, v45
	v_fmac_f32_e32 v41, v60, v45
	v_fmac_f32_e32 v42, v59, v45
	v_fmac_f32_e32 v43, v58, v45
	v_fmac_f32_e32 v44, v57, v45
	s_waitcnt lgkmcnt(11)
	v_lshlrev_b32_e32 v45, 16, v103
	ds_read_u16 v103, v22 offset:32768
	v_fmac_f32_e32 v29, v73, v45
	v_fmac_f32_e32 v30, v72, v45
	v_fmac_f32_e32 v31, v71, v45
	v_fmac_f32_e32 v32, v70, v45
	v_fmac_f32_e32 v33, v69, v45
	v_fmac_f32_e32 v34, v68, v45
	v_fmac_f32_e32 v35, v67, v45
	v_fmac_f32_e32 v36, v66, v45
	v_fmac_f32_e32 v37, v65, v45
	v_fmac_f32_e32 v38, v64, v45
	v_fmac_f32_e32 v39, v63, v45
	v_fmac_f32_e32 v40, v62, v45
	v_fmac_f32_e32 v41, v61, v45
	v_fmac_f32_e32 v42, v60, v45
	v_fmac_f32_e32 v43, v59, v45
	v_fmac_f32_e32 v44, v58, v45
	s_waitcnt lgkmcnt(11)
	v_lshlrev_b32_e32 v45, 16, v104
	ds_read_u16 v104, v22 offset:33792
	v_fmac_f32_e32 v29, v74, v45
	v_fmac_f32_e32 v30, v73, v45
	v_fmac_f32_e32 v31, v72, v45
	v_fmac_f32_e32 v32, v71, v45
	v_fmac_f32_e32 v33, v70, v45
	v_fmac_f32_e32 v34, v69, v45
	v_fmac_f32_e32 v35, v68, v45
	v_fmac_f32_e32 v36, v67, v45
	v_fmac_f32_e32 v37, v66, v45
	v_fmac_f32_e32 v38, v65, v45
	v_fmac_f32_e32 v39, v64, v45
	v_fmac_f32_e32 v40, v63, v45
	v_fmac_f32_e32 v41, v62, v45
	v_fmac_f32_e32 v42, v61, v45
	v_fmac_f32_e32 v43, v60, v45
	v_fmac_f32_e32 v44, v59, v45
	s_waitcnt lgkmcnt(11)
	v_lshlrev_b32_e32 v45, 16, v105
	ds_read_u16 v105, v22 offset:34816
	v_fmac_f32_e32 v29, v75, v45
	v_fmac_f32_e32 v30, v74, v45
	v_fmac_f32_e32 v31, v73, v45
	v_fmac_f32_e32 v32, v72, v45
	v_fmac_f32_e32 v33, v71, v45
	v_fmac_f32_e32 v34, v70, v45
	v_fmac_f32_e32 v35, v69, v45
	v_fmac_f32_e32 v36, v68, v45
	v_fmac_f32_e32 v37, v67, v45
	v_fmac_f32_e32 v38, v66, v45
	v_fmac_f32_e32 v39, v65, v45
	v_fmac_f32_e32 v40, v64, v45
	v_fmac_f32_e32 v41, v63, v45
	v_fmac_f32_e32 v42, v62, v45
	v_fmac_f32_e32 v43, v61, v45
	v_fmac_f32_e32 v44, v60, v45
	s_waitcnt lgkmcnt(11)
	v_lshlrev_b32_e32 v45, 16, v106
	ds_read_u16 v106, v22 offset:35840
	v_fmac_f32_e32 v29, v76, v45
	v_fmac_f32_e32 v30, v75, v45
	v_fmac_f32_e32 v31, v74, v45
	v_fmac_f32_e32 v32, v73, v45
	v_fmac_f32_e32 v33, v72, v45
	v_fmac_f32_e32 v34, v71, v45
	v_fmac_f32_e32 v35, v70, v45
	v_fmac_f32_e32 v36, v69, v45
	v_fmac_f32_e32 v37, v68, v45
	v_fmac_f32_e32 v38, v67, v45
	v_fmac_f32_e32 v39, v66, v45
	v_fmac_f32_e32 v40, v65, v45
	v_fmac_f32_e32 v41, v64, v45
	v_fmac_f32_e32 v42, v63, v45
	v_fmac_f32_e32 v43, v62, v45
	v_fmac_f32_e32 v44, v61, v45
	s_waitcnt lgkmcnt(11)
	v_lshlrev_b32_e32 v45, 16, v107
	ds_read_u16 v107, v22 offset:36864
	v_fmac_f32_e32 v29, v77, v45
	v_fmac_f32_e32 v30, v76, v45
	v_fmac_f32_e32 v31, v75, v45
	v_fmac_f32_e32 v32, v74, v45
	v_fmac_f32_e32 v33, v73, v45
	v_fmac_f32_e32 v34, v72, v45
	v_fmac_f32_e32 v35, v71, v45
	v_fmac_f32_e32 v36, v70, v45
	v_fmac_f32_e32 v37, v69, v45
	v_fmac_f32_e32 v38, v68, v45
	v_fmac_f32_e32 v39, v67, v45
	v_fmac_f32_e32 v40, v66, v45
	v_fmac_f32_e32 v41, v65, v45
	v_fmac_f32_e32 v42, v64, v45
	v_fmac_f32_e32 v43, v63, v45
	v_fmac_f32_e32 v44, v62, v45
	s_waitcnt lgkmcnt(11)
	v_lshlrev_b32_e32 v45, 16, v108
	ds_read_u16 v108, v22 offset:37888
	v_fmac_f32_e32 v29, v78, v45
	v_fmac_f32_e32 v30, v77, v45
	v_fmac_f32_e32 v31, v76, v45
	v_fmac_f32_e32 v32, v75, v45
	v_fmac_f32_e32 v33, v74, v45
	v_fmac_f32_e32 v34, v73, v45
	v_fmac_f32_e32 v35, v72, v45
	v_fmac_f32_e32 v36, v71, v45
	v_fmac_f32_e32 v37, v70, v45
	v_fmac_f32_e32 v38, v69, v45
	v_fmac_f32_e32 v39, v68, v45
	v_fmac_f32_e32 v40, v67, v45
	v_fmac_f32_e32 v41, v66, v45
	v_fmac_f32_e32 v42, v65, v45
	v_fmac_f32_e32 v43, v64, v45
	v_fmac_f32_e32 v44, v63, v45
	s_waitcnt lgkmcnt(11)
	v_lshlrev_b32_e32 v45, 16, v109
	ds_read_u16 v109, v22 offset:38912
	v_fmac_f32_e32 v29, v79, v45
	v_fmac_f32_e32 v30, v78, v45
	v_fmac_f32_e32 v31, v77, v45
	v_fmac_f32_e32 v32, v76, v45
	v_fmac_f32_e32 v33, v75, v45
	v_fmac_f32_e32 v34, v74, v45
	v_fmac_f32_e32 v35, v73, v45
	v_fmac_f32_e32 v36, v72, v45
	v_fmac_f32_e32 v37, v71, v45
	v_fmac_f32_e32 v38, v70, v45
	v_fmac_f32_e32 v39, v69, v45
	v_fmac_f32_e32 v40, v68, v45
	v_fmac_f32_e32 v41, v67, v45
	v_fmac_f32_e32 v42, v66, v45
	v_fmac_f32_e32 v43, v65, v45
	v_fmac_f32_e32 v44, v64, v45
	s_waitcnt lgkmcnt(11)
	v_lshlrev_b32_e32 v45, 16, v110
	ds_read_u16 v110, v22 offset:39936
	v_fmac_f32_e32 v29, v80, v45
	v_fmac_f32_e32 v30, v79, v45
	v_fmac_f32_e32 v31, v78, v45
	v_fmac_f32_e32 v32, v77, v45
	v_fmac_f32_e32 v33, v76, v45
	v_fmac_f32_e32 v34, v75, v45
	v_fmac_f32_e32 v35, v74, v45
	v_fmac_f32_e32 v36, v73, v45
	v_fmac_f32_e32 v37, v72, v45
	v_fmac_f32_e32 v38, v71, v45
	v_fmac_f32_e32 v39, v70, v45
	v_fmac_f32_e32 v40, v69, v45
	v_fmac_f32_e32 v41, v68, v45
	v_fmac_f32_e32 v42, v67, v45
	v_fmac_f32_e32 v43, v66, v45
	v_fmac_f32_e32 v44, v65, v45
	s_waitcnt lgkmcnt(11)
	v_lshlrev_b32_e32 v45, 16, v111
	ds_read_u16 v111, v22 offset:40960
	v_fmac_f32_e32 v29, v81, v45
	v_fmac_f32_e32 v30, v80, v45
	v_fmac_f32_e32 v31, v79, v45
	v_fmac_f32_e32 v32, v78, v45
	v_fmac_f32_e32 v33, v77, v45
	v_fmac_f32_e32 v34, v76, v45
	v_fmac_f32_e32 v35, v75, v45
	v_fmac_f32_e32 v36, v74, v45
	v_fmac_f32_e32 v37, v73, v45
	v_fmac_f32_e32 v38, v72, v45
	v_fmac_f32_e32 v39, v71, v45
	v_fmac_f32_e32 v40, v70, v45
	v_fmac_f32_e32 v41, v69, v45
	v_fmac_f32_e32 v42, v68, v45
	v_fmac_f32_e32 v43, v67, v45
	v_fmac_f32_e32 v44, v66, v45
	s_waitcnt lgkmcnt(11)
	v_lshlrev_b32_e32 v45, 16, v100
	ds_read_u16 v100, v22 offset:41984
	v_fmac_f32_e32 v29, v82, v45
	v_fmac_f32_e32 v30, v81, v45
	v_fmac_f32_e32 v31, v80, v45
	v_fmac_f32_e32 v32, v79, v45
	v_fmac_f32_e32 v33, v78, v45
	v_fmac_f32_e32 v34, v77, v45
	v_fmac_f32_e32 v35, v76, v45
	v_fmac_f32_e32 v36, v75, v45
	v_fmac_f32_e32 v37, v74, v45
	v_fmac_f32_e32 v38, v73, v45
	v_fmac_f32_e32 v39, v72, v45
	v_fmac_f32_e32 v40, v71, v45
	v_fmac_f32_e32 v41, v70, v45
	v_fmac_f32_e32 v42, v69, v45
	v_fmac_f32_e32 v43, v68, v45
	v_fmac_f32_e32 v44, v67, v45
	s_waitcnt lgkmcnt(11)
	v_lshlrev_b32_e32 v45, 16, v101
	ds_read_u16 v101, v22 offset:43008
	v_fmac_f32_e32 v29, v83, v45
	v_fmac_f32_e32 v30, v82, v45
	v_fmac_f32_e32 v31, v81, v45
	v_fmac_f32_e32 v32, v80, v45
	v_fmac_f32_e32 v33, v79, v45
	v_fmac_f32_e32 v34, v78, v45
	v_fmac_f32_e32 v35, v77, v45
	v_fmac_f32_e32 v36, v76, v45
	v_fmac_f32_e32 v37, v75, v45
	v_fmac_f32_e32 v38, v74, v45
	v_fmac_f32_e32 v39, v73, v45
	v_fmac_f32_e32 v40, v72, v45
	v_fmac_f32_e32 v41, v71, v45
	v_fmac_f32_e32 v42, v70, v45
	v_fmac_f32_e32 v43, v69, v45
	v_fmac_f32_e32 v44, v68, v45
	s_waitcnt lgkmcnt(11)
	v_lshlrev_b32_e32 v45, 16, v102
	ds_read_u16 v102, v22 offset:44032
	v_fmac_f32_e32 v30, v83, v45
	v_fmac_f32_e32 v31, v82, v45
	v_fmac_f32_e32 v32, v81, v45
	v_fmac_f32_e32 v33, v80, v45
	v_fmac_f32_e32 v34, v79, v45
	v_fmac_f32_e32 v35, v78, v45
	v_fmac_f32_e32 v36, v77, v45
	v_fmac_f32_e32 v37, v76, v45
	v_fmac_f32_e32 v38, v75, v45
	v_fmac_f32_e32 v39, v74, v45
	v_fmac_f32_e32 v40, v73, v45
	v_fmac_f32_e32 v41, v72, v45
	v_fmac_f32_e32 v42, v71, v45
	v_fmac_f32_e32 v43, v70, v45
	v_fmac_f32_e32 v44, v69, v45
	s_waitcnt lgkmcnt(11)
	v_lshlrev_b32_e32 v45, 16, v103
	ds_read_u16 v103, v22 offset:45056
	v_fmac_f32_e32 v31, v83, v45
	v_fmac_f32_e32 v32, v82, v45
	v_fmac_f32_e32 v33, v81, v45
	v_fmac_f32_e32 v34, v80, v45
	v_fmac_f32_e32 v35, v79, v45
	v_fmac_f32_e32 v36, v78, v45
	v_fmac_f32_e32 v37, v77, v45
	v_fmac_f32_e32 v38, v76, v45
	v_fmac_f32_e32 v39, v75, v45
	v_fmac_f32_e32 v40, v74, v45
	v_fmac_f32_e32 v41, v73, v45
	v_fmac_f32_e32 v42, v72, v45
	v_fmac_f32_e32 v43, v71, v45
	v_fmac_f32_e32 v44, v70, v45
	s_waitcnt lgkmcnt(11)
	v_lshlrev_b32_e32 v45, 16, v104
	ds_read_u16 v104, v22 offset:46080
	v_fmac_f32_e32 v32, v83, v45
	v_fmac_f32_e32 v33, v82, v45
	v_fmac_f32_e32 v34, v81, v45
	v_fmac_f32_e32 v35, v80, v45
	v_fmac_f32_e32 v36, v79, v45
	v_fmac_f32_e32 v37, v78, v45
	v_fmac_f32_e32 v38, v77, v45
	v_fmac_f32_e32 v39, v76, v45
	v_fmac_f32_e32 v40, v75, v45
	v_fmac_f32_e32 v41, v74, v45
	v_fmac_f32_e32 v42, v73, v45
	v_fmac_f32_e32 v43, v72, v45
	v_fmac_f32_e32 v44, v71, v45
	s_waitcnt lgkmcnt(11)
	v_lshlrev_b32_e32 v45, 16, v105
	v_fmac_f32_e32 v33, v83, v45
	v_fmac_f32_e32 v34, v82, v45
	v_fmac_f32_e32 v35, v81, v45
	v_fmac_f32_e32 v36, v80, v45
	v_fmac_f32_e32 v37, v79, v45
	v_fmac_f32_e32 v38, v78, v45
	v_fmac_f32_e32 v39, v77, v45
	v_fmac_f32_e32 v40, v76, v45
	v_fmac_f32_e32 v41, v75, v45
	v_fmac_f32_e32 v42, v74, v45
	v_fmac_f32_e32 v43, v73, v45
	v_fmac_f32_e32 v44, v72, v45
	s_waitcnt lgkmcnt(10)
	v_lshlrev_b32_e32 v45, 16, v106
	v_fmac_f32_e32 v34, v83, v45
	v_fmac_f32_e32 v35, v82, v45
	v_fmac_f32_e32 v36, v81, v45
	v_fmac_f32_e32 v37, v80, v45
	v_fmac_f32_e32 v38, v79, v45
	v_fmac_f32_e32 v39, v78, v45
	v_fmac_f32_e32 v40, v77, v45
	v_fmac_f32_e32 v41, v76, v45
	v_fmac_f32_e32 v42, v75, v45
	v_fmac_f32_e32 v43, v74, v45
	v_fmac_f32_e32 v44, v73, v45
	s_waitcnt lgkmcnt(9)
	v_lshlrev_b32_e32 v45, 16, v107
	v_fmac_f32_e32 v35, v83, v45
	v_fmac_f32_e32 v36, v82, v45
	v_fmac_f32_e32 v37, v81, v45
	v_fmac_f32_e32 v38, v80, v45
	v_fmac_f32_e32 v39, v79, v45
	v_fmac_f32_e32 v40, v78, v45
	v_fmac_f32_e32 v41, v77, v45
	v_fmac_f32_e32 v42, v76, v45
	v_fmac_f32_e32 v43, v75, v45
	v_fmac_f32_e32 v44, v74, v45
	s_waitcnt lgkmcnt(8)
	v_lshlrev_b32_e32 v45, 16, v108
	v_fmac_f32_e32 v36, v83, v45
	v_fmac_f32_e32 v37, v82, v45
	v_fmac_f32_e32 v38, v81, v45
	v_fmac_f32_e32 v39, v80, v45
	v_fmac_f32_e32 v40, v79, v45
	v_fmac_f32_e32 v41, v78, v45
	v_fmac_f32_e32 v42, v77, v45
	v_fmac_f32_e32 v43, v76, v45
	v_fmac_f32_e32 v44, v75, v45
	s_waitcnt lgkmcnt(7)
	v_lshlrev_b32_e32 v45, 16, v109
	v_fmac_f32_e32 v37, v83, v45
	v_fmac_f32_e32 v38, v82, v45
	v_fmac_f32_e32 v39, v81, v45
	v_fmac_f32_e32 v40, v80, v45
	v_fmac_f32_e32 v41, v79, v45
	v_fmac_f32_e32 v42, v78, v45
	v_fmac_f32_e32 v43, v77, v45
	v_fmac_f32_e32 v44, v76, v45
	s_waitcnt lgkmcnt(6)
	v_lshlrev_b32_e32 v45, 16, v110
	v_fmac_f32_e32 v38, v83, v45
	v_fmac_f32_e32 v39, v82, v45
	v_fmac_f32_e32 v40, v81, v45
	v_fmac_f32_e32 v41, v80, v45
	v_fmac_f32_e32 v42, v79, v45
	v_fmac_f32_e32 v43, v78, v45
	v_fmac_f32_e32 v44, v77, v45
	s_waitcnt lgkmcnt(5)
	v_lshlrev_b32_e32 v45, 16, v111
	v_fmac_f32_e32 v39, v83, v45
	v_fmac_f32_e32 v40, v82, v45
	v_fmac_f32_e32 v41, v81, v45
	v_fmac_f32_e32 v42, v80, v45
	v_fmac_f32_e32 v43, v79, v45
	v_fmac_f32_e32 v44, v78, v45
	s_waitcnt lgkmcnt(4)
	v_lshlrev_b32_e32 v45, 16, v100
	v_fmac_f32_e32 v40, v83, v45
	v_fmac_f32_e32 v41, v82, v45
	v_fmac_f32_e32 v42, v81, v45
	v_fmac_f32_e32 v43, v80, v45
	v_fmac_f32_e32 v44, v79, v45
	s_waitcnt lgkmcnt(3)
	v_lshlrev_b32_e32 v45, 16, v101
	v_fmac_f32_e32 v41, v83, v45
	v_fmac_f32_e32 v42, v82, v45
	v_fmac_f32_e32 v43, v81, v45
	v_fmac_f32_e32 v44, v80, v45
	s_waitcnt lgkmcnt(2)
	v_lshlrev_b32_e32 v45, 16, v102
	v_fmac_f32_e32 v42, v83, v45
	v_fmac_f32_e32 v43, v82, v45
	v_fmac_f32_e32 v44, v81, v45
	s_waitcnt lgkmcnt(1)
	v_lshlrev_b32_e32 v45, 16, v103
	v_fmac_f32_e32 v43, v83, v45
	v_fmac_f32_e32 v44, v82, v45
	s_waitcnt lgkmcnt(0)
	v_lshlrev_b32_e32 v45, 16, v104
	v_fmac_f32_e32 v44, v83, v45
	ds_write2st64_b32 v23, v29, v30 offset1:8
	ds_write2st64_b32 v23, v31, v32 offset0:16 offset1:24
	ds_write2st64_b32 v23, v33, v34 offset0:32 offset1:40
	ds_write2st64_b32 v23, v35, v36 offset0:48 offset1:56
	ds_write2st64_b32 v23, v37, v38 offset0:64 offset1:72
	ds_write2st64_b32 v23, v39, v40 offset0:80 offset1:88
	ds_write2st64_b32 v23, v41, v42 offset0:96 offset1:104
	ds_write2st64_b32 v23, v43, v44 offset0:112 offset1:120
	v_add_u32_e32 v29, s36, v24
	v_cmp_gt_i32_e32 vcc, 64, v29
	s_waitcnt lgkmcnt(0)
	s_barrier
	s_and_saveexec_b64 s[34:35], vcc
	s_cbranch_execz .LBB0_2167
	ds_read_b128 v[30:33], v27
	ds_read_b128 v[34:37], v27 offset:16
	s_waitcnt lgkmcnt(1)
	v_mov_b32_e32 v38, v31
	v_mov_b32_e32 v39, v32
	v_mov_b32_e32 v40, v30
	v_mov_b32_e32 v41, v33
	v_pk_add_f32 v[38:39], v[38:39], v[40:41]
	s_waitcnt lgkmcnt(0)
	v_mov_b32_e32 v40, v36
	v_mov_b32_e32 v41, v34
	v_mov_b32_e32 v42, v37
	v_mov_b32_e32 v43, v35
	v_pk_add_f32 v[40:41], v[40:41], v[42:43]
	v_add_f32_e32 v29, v38, v39
	v_add_f32_e32 v29, v29, v41
	v_add_f32_e32 v29, v40, v29
	v_and_b32_e32 v39, 64, v214
	v_xor_b32_e32 v38, 16, v214
	v_add_f32_dpp v29, v29, v29 quad_perm:[1,0,3,2] row_mask:0xf bank_mask:0xf bound_ctrl:1
	v_add_u32_e32 v39, 64, v39
	v_cmp_lt_i32_e32 vcc, v38, v39
	v_add_f32_dpp v29, v29, v29 quad_perm:[2,3,0,1] row_mask:0xf bank_mask:0xf bound_ctrl:1
	s_nop 0
	v_cndmask_b32_e32 v38, v214, v38, vcc
	v_add_f32_dpp v29, v29, v29 row_half_mirror row_mask:0xf bank_mask:0xf bound_ctrl:1
	v_lshlrev_b32_e32 v46, 2, v38
	s_nop 0
	v_add_f32_dpp v29, v29, v29 row_mirror row_mask:0xf bank_mask:0xf bound_ctrl:1
	ds_bpermute_b32 v38, v46, v29
	s_waitcnt lgkmcnt(0)
	v_add_f32_e32 v29, v29, v38
	v_xor_b32_e32 v38, 32, v214
	v_cmp_lt_i32_e32 vcc, v38, v39
	s_nop 1
	v_cndmask_b32_e32 v38, v214, v38, vcc
	v_lshlrev_b32_e32 v47, 2, v38
	ds_bpermute_b32 v38, v47, v29
	s_waitcnt lgkmcnt(0)
	v_add_f32_e32 v29, v29, v38
	v_fmamk_f32 v31, v29, 0xbb000000, v31
	v_fmamk_f32 v30, v29, 0xbb000000, v30
	v_fmamk_f32 v33, v29, 0xbb000000, v33
	v_fmac_f32_e32 v32, 0xbb000000, v29
	v_pk_mul_f32 v[38:39], v[32:33], v[32:33]
	v_pk_mul_f32 v[40:41], v[30:31], v[30:31]
	v_fmamk_f32 v35, v29, 0xbb000000, v35
	v_fmamk_f32 v34, v29, 0xbb000000, v34
	v_fmamk_f32 v37, v29, 0xbb000000, v37
	v_fmac_f32_e32 v36, 0xbb000000, v29
	v_pk_mov_b32 v[42:43], v[40:41], v[38:39] op_sel:[1,0]
	v_mov_b32_e32 v41, v39
	v_pk_add_f32 v[38:39], v[42:43], v[40:41]
	v_pk_mul_f32 v[40:41], v[36:37], v[36:37]
	v_pk_mul_f32 v[42:43], v[34:35], v[34:35]
	v_mov_b32_e32 v44, v40
	v_mov_b32_e32 v45, v42
	v_mov_b32_e32 v42, v41
	v_pk_add_f32 v[40:41], v[44:45], v[42:43]
	v_add_f32_e32 v29, v38, v39
	v_add_f32_e32 v29, v41, v29
	v_add_f32_e32 v29, v40, v29
	s_nop 1
	v_add_f32_dpp v29, v29, v29 quad_perm:[1,0,3,2] row_mask:0xf bank_mask:0xf bound_ctrl:1
	s_nop 1
	v_add_f32_dpp v29, v29, v29 quad_perm:[2,3,0,1] row_mask:0xf bank_mask:0xf bound_ctrl:1
	s_nop 1
	v_add_f32_dpp v29, v29, v29 row_half_mirror row_mask:0xf bank_mask:0xf bound_ctrl:1
	s_nop 1
	v_add_f32_dpp v29, v29, v29 row_mirror row_mask:0xf bank_mask:0xf bound_ctrl:1
	ds_bpermute_b32 v38, v46, v29
	s_waitcnt lgkmcnt(0)
	v_add_f32_e32 v29, v29, v38
	ds_bpermute_b32 v38, v47, v29
	s_waitcnt lgkmcnt(0)
	v_add_f32_e32 v29, v29, v38
	v_fmamk_f32 v29, v29, 0x3b000000, v1
	v_mul_f32_e32 v38, 0x4b800000, v29
	v_cmp_gt_f32_e32 vcc, s77, v29
	s_nop 1
	v_cndmask_b32_e32 v29, v29, v38, vcc
	v_rsq_f32_e32 v29, v29
	s_nop 0
	v_mul_f32_e32 v38, 0x45800000, v29
	v_cndmask_b32_e32 v38, v29, v38, vcc
	v_pk_mul_f32 v[30:31], v[30:31], v[38:39] op_sel_hi:[1,0]
	v_pk_mul_f32 v[34:35], v[34:35], v[38:39] op_sel_hi:[1,0]
	v_pk_fma_f32 v[30:31], v[6:7], v[30:31], v[14:15]
	v_pk_fma_f32 v[34:35], v[2:3], v[34:35], v[10:11]
	v_mul_f32_e32 v29, 0xbfb8aa3b, v30
	v_pk_mul_f32 v[32:33], v[32:33], v[38:39] op_sel_hi:[1,0]
	v_pk_mul_f32 v[36:37], v[36:37], v[38:39] op_sel_hi:[1,0]
	v_exp_f32_e32 v29, v29
	v_mul_f32_e32 v38, 0xbfb8aa3b, v34
	v_exp_f32_e32 v39, v38
	v_mul_f32_e32 v40, 0xbfb8aa3b, v35
	v_add_f32_e32 v29, 1.0, v29
	v_rcp_f32_e32 v38, v29
	v_add_f32_e32 v29, 1.0, v39
	v_mul_f32_e32 v39, 0xbfb8aa3b, v31
	v_exp_f32_e32 v39, v39
	v_exp_f32_e32 v41, v40
	v_pk_fma_f32 v[32:33], v[8:9], v[32:33], v[16:17]
	v_rcp_f32_e32 v40, v29
	v_add_f32_e32 v29, 1.0, v39
	v_pk_fma_f32 v[36:37], v[4:5], v[36:37], v[12:13]
	v_rcp_f32_e32 v39, v29
	v_add_f32_e32 v29, 1.0, v41
	v_mul_f32_e32 v41, 0xbfb8aa3b, v32
	v_exp_f32_e32 v42, v41
	v_mul_f32_e32 v41, 0xbfb8aa3b, v36
	v_exp_f32_e32 v43, v41
	v_rcp_f32_e32 v41, v29
	v_add_f32_e32 v29, 1.0, v42
	v_rcp_f32_e32 v42, v29
	v_add_f32_e32 v29, 1.0, v43
	v_mul_f32_e32 v43, 0xbfb8aa3b, v33
	v_exp_f32_e32 v43, v43
	v_mul_f32_e32 v44, 0xbfb8aa3b, v37
	v_exp_f32_e32 v45, v44
	v_rcp_f32_e32 v44, v29
	v_add_f32_e32 v29, 1.0, v43
	v_rcp_f32_e32 v43, v29
	v_add_f32_e32 v29, 1.0, v45
	v_rcp_f32_e32 v45, v29
	v_pk_mul_f32 v[30:31], v[30:31], v[38:39]
	v_pk_mul_f32 v[34:35], v[34:35], v[40:41]
	v_pk_mul_f32 v[32:33], v[32:33], v[42:43]
	v_cvt_pk_bf16_f32 v30, v30, v31
	v_cvt_pk_bf16_f32 v31, v32, v33
	v_cvt_pk_bf16_f32 v32, v34, v35
	v_add_u32_e32 v34, s36, v26
	v_ashrrev_i32_e32 v35, 31, v34
	v_pk_mul_f32 v[36:37], v[36:37], v[44:45]
	v_lshlrev_b64 v[34:35], 11, v[34:35]
	v_cvt_pk_bf16_f32 v33, v36, v37
	v_lshl_add_u64 v[34:35], v[18:19], 0, v[34:35]
	global_store_dwordx4 v[34:35], v[30:33], off offset:1024
